# MP0: per-tile message-row-0 mask (v_cmp + 4 v_cndmask per wave-tile) removed from the loop; workgroup 0 re-zeroes row 0 once at kernel end
# speedup vs baseline: 1.0041x; 1.0012x over previous
_Z10mp2_kernelILb0ELi0EEvPKDF16_PDF16_PKiPKfPKDv8_DF16_S6_S6_ii:
	s_load_dwordx4 s[8:11], s[0:1], 0x20
	s_load_dwordx2 s[14:15], s[0:1], 0x30
	v_readfirstlane_b32 s27, v0
	s_lshr_b32 s28, s27, 6
	s_mov_b32 s42, s28
	s_mov_b32 s43, s2
	s_mul_i32 s4, s28, 29
	s_mov_b32 s5, 0
	s_lshl_b64 s[4:5], s[4:5], 10
	v_and_b32_e32 v1, 63, v0
	s_waitcnt lgkmcnt(0)
	s_add_u32 s4, s8, s4
	s_addc_u32 s5, s9, s5
	v_lshlrev_b32_e32 v150, 4, v1
	v_mov_b32_e32 v151, 0
	v_lshl_add_u64 v[34:35], s[4:5], 0, v[150:151]
	s_movk_i32 s3, 0x1000
	v_add_co_u32_e32 v94, vcc, s3, v34
	s_movk_i32 s3, 0x2000
	s_nop 0
	v_addc_co_u32_e32 v95, vcc, 0, v35, vcc
	v_add_co_u32_e32 v118, vcc, s3, v34
	s_movk_i32 s3, 0x3000
	s_nop 0
	v_addc_co_u32_e32 v119, vcc, 0, v35, vcc
	v_add_co_u32_e32 v96, vcc, s3, v34
	s_movk_i32 s3, 0x4000
	s_nop 0
	v_addc_co_u32_e32 v97, vcc, 0, v35, vcc
	v_add_co_u32_e32 v98, vcc, s3, v34
	s_movk_i32 s3, 0x5000
	s_nop 0
	v_addc_co_u32_e32 v99, vcc, 0, v35, vcc
	v_add_co_u32_e32 v100, vcc, s3, v34
	s_movk_i32 s3, 0x6000
	s_nop 0
	v_addc_co_u32_e32 v101, vcc, 0, v35, vcc
	v_add_co_u32_e32 v102, vcc, s3, v34
	global_load_dwordx4 v[2:5], v[94:95], off offset:1024
	global_load_dwordx4 v[6:9], v[94:95], off offset:2048
	v_addc_co_u32_e32 v103, vcc, 0, v35, vcc
	v_add_co_u32_e32 v120, vcc, 0x7000, v34
	global_load_dwordx4 v[10:13], v[118:119], off
	global_load_dwordx4 v[14:17], v[118:119], off offset:1024
	global_load_dwordx4 v[18:21], v[96:97], off offset:3072
	global_load_dwordx4 v[22:25], v[98:99], off offset:1024
	global_load_dwordx4 v[26:29], v[118:119], off offset:2048
	global_load_dwordx4 v[30:33], v[118:119], off offset:3072
	v_addc_co_u32_e32 v121, vcc, 0, v35, vcc
	global_load_dwordx4 v[34:37], v[98:99], off offset:2048
	global_load_dwordx4 v[38:41], v[98:99], off offset:3072
	global_load_dwordx4 v[42:45], v[96:97], off offset:1024
	global_load_dwordx4 v[46:49], v[96:97], off offset:2048
	global_load_dwordx4 v[50:53], v[94:95], off offset:3072
	global_load_dwordx4 v[54:57], v[96:97], off
	global_load_dwordx4 v[58:61], v[100:101], off offset:-4096
	global_load_dwordx4 v[62:65], v[100:101], off
	global_load_dwordx4 v[66:69], v[100:101], off offset:1024
	global_load_dwordx4 v[70:73], v[100:101], off offset:2048
	global_load_dwordx4 v[74:77], v[100:101], off offset:3072
	global_load_dwordx4 v[78:81], v[102:103], off offset:2048
	global_load_dwordx4 v[82:85], v[102:103], off offset:3072
	global_load_dwordx4 v[86:89], v[102:103], off offset:1024
	global_load_dwordx4 v[90:93], v[102:103], off
	global_load_dwordx4 v[94:97], v[120:121], off
	global_load_dwordx4 v[98:101], v150, s[4:5]
	s_nop 0
	global_load_dwordx4 v[102:105], v[118:119], off offset:-4096
	global_load_dwordx4 v[106:109], v150, s[4:5] offset:3072
	global_load_dwordx4 v[110:113], v150, s[4:5] offset:1024
	global_load_dwordx4 v[114:117], v150, s[4:5] offset:2048
	s_movk_i32 s3, 0x80
	v_cmp_gt_u32_e32 vcc, s3, v0
	s_and_saveexec_b64 s[4:5], vcc
	s_cbranch_execnz .LBB5_4
	s_or_b64 exec, exec, s[4:5]
	v_cmp_gt_u32_e32 vcc, 64, v0
	s_and_saveexec_b64 s[4:5], vcc
	s_cbranch_execnz .LBB5_5

.LBB5_14:
	v_or_b32_e32 v0, s33, v200
	ds_read_b128 v[142:145], v0 offset:0
	s_waitcnt lgkmcnt(4)
	s_nop 0
	v_mfma_f32_16x16x32_f16 v[134:137], v[114:117], v[134:137], v[166:169]
	ds_read_b128 v[146:149], v0 offset:0x1000
	s_waitcnt lgkmcnt(4)
	s_nop 0
	v_mfma_f32_16x16x32_f16 v[138:141], v[114:117], v[138:141], v[170:173]
	ds_read_b128 v[150:153], v0 offset:0x2000
	s_waitcnt lgkmcnt(4)
	s_nop 0
	v_mfma_f32_16x16x32_f16 v[154:157], v[114:117], v[158:161], v[174:177]
	ds_read_b128 v[158:161], v0 offset:0x3000
	s_waitcnt lgkmcnt(4)
	s_nop 0
	v_mfma_f32_16x16x32_f16 v[162:165], v[114:117], v[162:165], v[178:181]
	ds_read_b128 v[166:169], v205 offset:0
	s_waitcnt lgkmcnt(4)
	s_nop 0
	v_mfma_f32_16x16x32_f16 v[134:137], v[106:109], v[142:145], v[134:137]
	ds_read_b128 v[142:145], v205 offset:0x100
	s_waitcnt lgkmcnt(4)
	s_nop 0
	v_mfma_f32_16x16x32_f16 v[138:141], v[106:109], v[146:149], v[138:141]
	ds_read_b128 v[146:149], v205 offset:0x200
	s_waitcnt lgkmcnt(4)
	s_nop 0
	v_mfma_f32_16x16x32_f16 v[150:153], v[106:109], v[150:153], v[154:157]
	ds_read_b128 v[154:157], v205 offset:0x300
	s_waitcnt lgkmcnt(4)
	s_nop 0
	v_mfma_f32_16x16x32_f16 v[158:161], v[106:109], v[158:161], v[162:165]
	s_waitcnt lgkmcnt(3)
	s_nop 0
	v_mfma_f32_16x16x32_f16 v[134:137], v[102:105], v[166:169], v[134:137]
	s_waitcnt lgkmcnt(2)
	s_nop 0
	v_mfma_f32_16x16x32_f16 v[138:141], v[102:105], v[142:145], v[138:141]
	s_waitcnt lgkmcnt(1)
	s_nop 0
	v_mfma_f32_16x16x32_f16 v[142:145], v[102:105], v[146:149], v[150:153]
	s_waitcnt lgkmcnt(0)
	s_nop 0
	v_mfma_f32_16x16x32_f16 v[146:149], v[102:105], v[154:157], v[158:161]
	s_nop 1
	v_cvt_pk_f16_f32 v1, v136, v137
	v_pk_max_f16 v1, v1, 0
	v_cvt_pk_f16_f32 v0, v134, v135
	v_pk_max_f16 v0, v0, 0
	v_cvt_pk_f16_f32 v135, v140, v141
	v_pk_max_f16 v135, v135, 0
	v_cvt_pk_f16_f32 v134, v138, v139
	v_pk_max_f16 v134, v134, 0
	ds_write2st64_b64 v218, v[0:1], v[134:135] offset1:8
	v_cvt_pk_f16_f32 v1, v144, v145
	v_pk_max_f16 v1, v1, 0
	v_cvt_pk_f16_f32 v0, v142, v143
	v_pk_max_f16 v0, v0, 0
	s_lshl_b32 s34, s2, 14
	v_cvt_pk_f16_f32 v135, v148, v149
	v_pk_max_f16 v135, v135, 0
	v_cvt_pk_f16_f32 v134, v146, v147
	v_pk_max_f16 v134, v134, 0
	s_or_b32 s34, s34, 0x18000
	ds_write2st64_b64 v218, v[0:1], v[134:135] offset0:16 offset1:24
	v_or_b32_e32 v172, s34, v197
	v_or_b32_e32 v223, s34, v198
	v_or_b32_e32 v143, s34, v199
	v_or_b32_e32 v142, s34, v200
	v_add_u32_e32 v0, s34, v208
	s_xor_b32 s34, s2, 1
	s_waitcnt vmcnt(2) lgkmcnt(0)
	s_barrier
	ds_read_b128 v[134:137], v201 offset:0
	s_mul_i32 s37, s34, 0xc000
	ds_read_b128 v[138:141], v202 offset:0
	ds_read_b128 v[144:147], v203 offset:0
	ds_read_b128 v[148:151], v204 offset:0
	v_add_u32_e32 v1, s37, v209
	ds_read_b128 v[152:155], v1 offset:0
	ds_read_b128 v[156:159], v1 offset:0x4000
	ds_read_b128 v[160:163], v1 offset:0x8000
	ds_read_b128 v[164:167], v1 offset:0x400
	ds_read_b128 v[168:171], v1 offset:0x4400
	ds_read_b128 v[174:177], v1 offset:0x8400
	ds_read_b128 v[178:181], v172 offset:0
	s_waitcnt lgkmcnt(10)
	v_subrev_u32_e32 v186, 56, v215
	v_mfma_f32_16x16x32_f16 v[182:185], v[2:5], v[134:137], v[118:121]
	v_min_u32_e32 v225, s17, v186
	v_add_u32_e32 v224, s20, v216
	v_mov_b32_e32 v230, s16
	v_mfma_f32_16x16x32_f16 v[186:189], v[42:45], v[134:137], v[122:125]
	v_cmp_gt_u32_e32 vcc, s8, v224
	ds_read_b128 v[226:229], v223 offset:0
	s_waitcnt lgkmcnt(10)
	v_mfma_f32_16x16x32_f16 v[134:137], v[66:69], v[134:137], v[126:129]
	v_lshl_or_b32 v173, v196, 8, v190
	v_cndmask_b32_e32 v230, v230, v224, vcc
	v_lshlrev_b32_e32 v234, 5, v230
	v_mfma_f32_16x16x32_f16 v[182:185], v[6:9], v[138:141], v[182:185]
	v_add_u32_e32 v196, -8, v215
	v_min_u32_e32 v238, s17, v196
	v_subrev_u32_e32 v196, 52, v215
	v_mfma_f32_16x16x32_f16 v[186:189], v[46:49], v[138:141], v[186:189]
	v_add_u32_e32 v221, -4, v215
	v_min_u32_e32 v196, s18, v196
	v_min_u32_e32 v221, s18, v221
	v_mfma_f32_16x16x32_f16 v[230:233], v[70:73], v[138:141], v[134:137]
	global_load_dwordx4 v[134:137], v234, s[6:7]
	global_load_dwordx4 v[138:141], v234, s[6:7] offset:16
	ds_read_b128 v[234:237], v143 offset:0
	s_waitcnt lgkmcnt(10)
	v_lshl_or_b32 v242, v192, 8, v190
	v_mfma_f32_16x16x32_f16 v[182:185], v[50:53], v[144:147], v[182:185]
	global_load_dword v192, v196, s[4:5]
	v_subrev_u32_e32 v239, 48, v215
	global_load_dword v221, v221, s[4:5]
	v_mfma_f32_16x16x32_f16 v[186:189], v[18:21], v[144:147], v[186:189]
	v_min_u32_e32 v222, s19, v215
	v_min_u32_e32 v239, s19, v239
	v_lshl_or_b32 v241, v194, 8, v191
	v_mfma_f32_16x16x32_f16 v[144:147], v[74:77], v[144:147], v[230:233]
	global_load_dword v196, v239, s[4:5]
	ds_read_b128 v[230:233], v142 offset:0
	s_waitcnt lgkmcnt(10)
	global_load_dword v194, v222, s[4:5]
	s_add_i32 s2, s28, s3
	v_mfma_f32_16x16x32_f16 v[182:185], v[10:13], v[148:151], v[182:185]
	v_lshl_or_b32 v243, v193, 8, v190
	global_load_dword v193, v225, s[4:5]
	s_min_i32 s35, s2, s14
	v_mfma_f32_16x16x32_f16 v[186:189], v[58:61], v[148:151], v[186:189]
	global_load_dword v222, v238, s[4:5]
	s_lshl_b32 s35, s35, 14
	s_lshl_b32 s34, s34, 14
	v_mfma_f32_16x16x32_f16 v[148:151], v[90:93], v[148:151], v[144:147]
	s_add_i32 s36, s33, 0
	v_add_u32_e32 v1, s35, v210
	s_add_i32 s38, s25, s34
	s_add_i32 s39, s36, s21
	s_add_i32 s40, s26, s34
	s_add_i32 s34, s36, s23
	s_add_i32 m0, s39, 0x8000
	v_add_u32_e32 v240, s35, v211
	s_add_i32 s41, s34, 0x8000
	s_add_i32 s35, s39, 0x4000
	s_add_i32 s36, s22, s33
	v_add_u32_e32 v239, s37, v212
	ds_read_b128 v[144:147], v201 offset:0x1000
	s_waitcnt lgkmcnt(4)
	s_waitcnt lgkmcnt(5)
	s_nop 0
	v_pk_add_f16 v152, v152, v156
	v_pk_add_f16 v153, v153, v157
	v_pk_add_f16 v154, v154, v158
	v_pk_add_f16 v155, v155, v159
	v_pk_add_f16 v154, v154, v162
	v_pk_add_f16 v155, v155, v163
	v_pk_add_f16 v153, v153, v161
	v_pk_add_f16 v152, v152, v160
	ds_write_b128 v239, v[152:155]
	v_pk_add_f16 v152, v164, v168
	v_pk_add_f16 v153, v165, v169
	v_pk_add_f16 v154, v166, v170
	v_pk_add_f16 v155, v167, v171
	v_pk_add_f16 v154, v154, v176
	v_pk_add_f16 v155, v155, v177
	v_pk_add_f16 v153, v153, v175
	v_pk_add_f16 v152, v152, v174
	ds_write_b128 v239, v[152:155] offset:1024
	ds_read_b128 v[152:155], v202 offset:0x1000
	s_waitcnt lgkmcnt(4)
	global_load_lds_dwordx4 v173, s[12:13]
	s_mov_b32 m0, s38
	ds_read_b128 v[168:171], v203 offset:0x1000
	s_waitcnt lgkmcnt(4)
	v_mfma_f32_16x16x32_f16 v[182:185], v[14:17], v[178:181], v[182:185]
	global_load_lds_dwordx4 v1, s[12:13]
	ds_read_b128 v[174:177], v204 offset:0x1000
	v_mfma_f32_16x16x32_f16 v[186:189], v[22:25], v[178:181], v[186:189]
	s_waitcnt lgkmcnt(4)
	v_mfma_f32_16x16x32_f16 v[178:181], v[86:89], v[178:181], v[130:133]
	v_mfma_f32_16x16x32_f16 v[156:159], v[26:29], v[226:229], v[182:185]
	v_mfma_f32_16x16x32_f16 v[160:163], v[34:37], v[226:229], v[186:189]
	v_mfma_f32_16x16x32_f16 v[164:167], v[78:81], v[226:229], v[178:181]
	v_mfma_f32_16x16x32_f16 v[156:159], v[30:33], v[234:237], v[156:159]
	v_mfma_f32_16x16x32_f16 v[160:163], v[38:41], v[234:237], v[160:163]
	v_mfma_f32_16x16x32_f16 v[164:167], v[82:85], v[234:237], v[164:167]
	v_mfma_f32_16x16x32_f16 v[156:159], v[54:57], v[230:233], v[156:159]
	v_mfma_f32_16x16x32_f16 v[160:163], v[62:65], v[230:233], v[160:163]
	v_mfma_f32_16x16x32_f16 v[164:167], v[94:97], v[230:233], v[164:167]
	s_mov_b32 m0, s41
	ds_read_b64 v[234:235], v0 offset:0
	ds_read_b128 v[178:181], v172 offset:0x1000
	s_waitcnt lgkmcnt(5)
	ds_read_b128 v[186:189], v223 offset:0x1000
	s_waitcnt lgkmcnt(5)
	s_nop 4
	v_exp_f32_e32 v1, v156
	s_waitcnt lgkmcnt(2)
	ds_read_b128 v[230:233], v143 offset:0x1000
	s_waitcnt lgkmcnt(5)
	global_load_lds_dwordx4 v241, s[12:13]
	v_add_f32_e32 v1, 1.0, v1
	v_rcp_f32_e32 v1, v1
	v_exp_f32_e32 v156, v160
	v_mfma_f32_16x16x32_f16 v[182:185], v[2:5], v[144:147], v[118:121]
	v_add_u32_e32 v225, v206, v213
	v_fma_f32 v1, v1, v164, v148
	v_exp_f32_e32 v1, v1
	v_add_f32_e32 v148, 1.0, v156
	v_exp_f32_e32 v156, v157
	v_rcp_f32_e32 v148, v148
	v_add_f32_e32 v1, 1.0, v1
	v_rcp_f32_e32 v1, v1
	v_add_f32_e32 v156, 1.0, v156
	v_rcp_f32_e32 v156, v156
	v_mfma_f32_16x16x32_f16 v[226:229], v[42:45], v[144:147], v[122:125]
	v_fma_f32 v1, v1, -2.0, 1.0
	v_fma_f32 v1, -v148, v1, v1
	v_fma_mixlo_f16 v1, v148, v234, v1 op_sel_hi:[0,1,0]
	v_mfma_f32_16x16x32_f16 v[144:147], v[66:69], v[144:147], v[126:129]
	v_exp_f32_e32 v148, v161
	v_fma_f32 v149, v156, v165, v149
	v_exp_f32_e32 v149, v149
	v_mfma_f32_16x16x32_f16 v[182:185], v[6:9], v[152:155], v[182:185]
	v_add_f32_e32 v148, 1.0, v148
	v_rcp_f32_e32 v156, v148
	v_add_f32_e32 v148, 1.0, v149
	v_mfma_f32_16x16x32_f16 v[226:229], v[46:49], v[152:155], v[226:229]
	v_rcp_f32_e32 v157, v148
	v_add_u32_e32 v173, 0x1000, v225
	v_mfma_f32_16x16x32_f16 v[144:147], v[70:73], v[152:155], v[144:147]
	v_mfma_f32_16x16x32_f16 v[152:155], v[50:53], v[168:171], v[182:185]
	v_mfma_f32_16x16x32_f16 v[182:185], v[18:21], v[168:171], v[226:229]
	v_mfma_f32_16x16x32_f16 v[144:147], v[74:77], v[168:171], v[144:147]
	ds_read_b128 v[168:171], v142 offset:0x1000
	s_waitcnt lgkmcnt(5)
	s_nop 0
	v_mfma_f32_16x16x32_f16 v[152:155], v[10:13], v[174:177], v[152:155]
	v_mfma_f32_16x16x32_f16 v[182:185], v[58:61], v[174:177], v[182:185]
	v_mfma_f32_16x16x32_f16 v[146:149], v[90:93], v[174:177], v[144:147]
	s_nop 3
	v_fma_f32 v144, v157, -2.0, 1.0
	v_fma_f32 v144, -v156, v144, v144
	v_fma_mixlo_f16 v144, v156, v234, v144 op_sel:[0,1,0] op_sel_hi:[0,1,0]
	s_mov_b32 m0, s40
	ds_read_b128 v[174:177], v201 offset:0x2000
	s_waitcnt lgkmcnt(4)
	ds_read_b128 v[226:229], v202 offset:0x2000
	s_waitcnt lgkmcnt(4)
	v_exp_f32_e32 v145, v158
	global_load_lds_dwordx4 v240, s[12:13]
	v_exp_f32_e32 v156, v162
	v_add_f32_e32 v145, 1.0, v145
	v_rcp_f32_e32 v145, v145
	v_mfma_f32_16x16x32_f16 v[152:155], v[14:17], v[178:181], v[152:155]
	v_pack_b32_f16 v144, v1, v144
	v_fma_f32 v145, v145, v166, v150
	v_add_f32_e32 v150, 1.0, v156
	v_rcp_f32_e32 v234, v150
	v_exp_f32_e32 v150, v159
	v_mfma_f32_16x16x32_f16 v[182:185], v[22:25], v[178:181], v[182:185]
	v_exp_f32_e32 v145, v145
	v_add_f32_e32 v150, 1.0, v150
	v_mfma_f32_16x16x32_f16 v[178:181], v[86:89], v[178:181], v[130:133]
	v_rcp_f32_e32 v150, v150
	v_add_f32_e32 v145, 1.0, v145
	v_rcp_f32_e32 v145, v145
	v_mfma_f32_16x16x32_f16 v[182:185], v[34:37], v[186:189], v[182:185]
	v_fmac_f32_e32 v151, v150, v167
	v_fma_f32 v145, v145, -2.0, 1.0
	v_mfma_f32_16x16x32_f16 v[178:181], v[78:81], v[186:189], v[178:181]
	v_fma_f32 v145, -v234, v145, v145
	v_fma_mixlo_f16 v145, v234, v235, v145 op_sel_hi:[0,1,0]
	v_mfma_f32_16x16x32_f16 v[152:155], v[26:29], v[186:189], v[152:155]
	ds_read_b128 v[186:189], v203 offset:0x2000
	s_waitcnt lgkmcnt(4)
	ds_read_b128 v[164:167], v204 offset:0x2000
	s_waitcnt lgkmcnt(4)
	s_nop 0
	v_mfma_f32_16x16x32_f16 v[156:159], v[38:41], v[230:233], v[182:185]
	s_nop 2
	v_exp_f32_e32 v182, v163
	v_mfma_f32_16x16x32_f16 v[160:163], v[82:85], v[230:233], v[178:181]
	s_nop 2
	v_exp_f32_e32 v178, v151
	v_mfma_f32_16x16x32_f16 v[152:155], v[30:33], v[230:233], v[152:155]
	v_add_f32_e32 v179, 1.0, v182
	v_add_f32_e32 v178, 1.0, v178
	v_mfma_f32_16x16x32_f16 v[150:153], v[54:57], v[168:171], v[152:155]
	v_mfma_f32_16x16x32_f16 v[154:157], v[62:65], v[168:171], v[156:159]
	s_nop 2
	v_rcp_f32_e32 v158, v178
	v_rcp_f32_e32 v159, v179
	v_mfma_f32_16x16x32_f16 v[168:171], v[94:97], v[168:171], v[160:163]
	v_fma_f32 v158, v158, -2.0, 1.0
	v_fma_f32 v158, -v159, v158, v158
	v_fma_mixlo_f16 v158, v159, v235, v158 op_sel:[0,1,0] op_sel_hi:[0,1,0]
	s_nop 0
	v_pack_b32_f16 v145, v145, v158
	global_store_dwordx2 v173, v[144:145], s[0:1] nt
	s_mov_b32 m0, s36
	ds_read_b64 v[238:239], v0 offset:0x1000
	ds_read_b128 v[178:181], v172 offset:0x2000
	s_waitcnt lgkmcnt(5)
	ds_read_b128 v[182:185], v223 offset:0x2000
	s_waitcnt lgkmcnt(5)
	v_exp_f32_e32 v1, v150
	s_waitcnt lgkmcnt(2)
	ds_read_b128 v[234:237], v143 offset:0x2000
	s_waitcnt lgkmcnt(5)
	global_load_lds_dwordx4 v243, s[12:13]
	v_add_f32_e32 v1, 1.0, v1
	v_rcp_f32_e32 v1, v1
	v_exp_f32_e32 v145, v151
	v_mfma_f32_16x16x32_f16 v[158:161], v[2:5], v[174:177], v[118:121]
	v_exp_f32_e32 v144, v154
	v_fma_f32 v1, v1, v168, v146
	v_exp_f32_e32 v1, v1
	v_mfma_f32_16x16x32_f16 v[230:233], v[42:45], v[174:177], v[122:125]
	v_add_f32_e32 v145, 1.0, v145
	v_rcp_f32_e32 v145, v145
	v_add_f32_e32 v1, 1.0, v1
	v_mfma_f32_16x16x32_f16 v[174:177], v[66:69], v[174:177], v[126:129]
	v_add_f32_e32 v144, 1.0, v144
	v_rcp_f32_e32 v1, v1
	v_rcp_f32_e32 v144, v144
	v_mfma_f32_16x16x32_f16 v[158:161], v[6:9], v[226:229], v[158:161]
	v_fma_f32 v145, v145, v169, v147
	v_exp_f32_e32 v145, v145
	v_exp_f32_e32 v146, v155
	v_mfma_f32_16x16x32_f16 v[174:177], v[70:73], v[226:229], v[174:177]
	v_fma_f32 v1, v1, -2.0, 1.0
	v_fma_f32 v1, -v144, v1, v1
	v_fma_mixlo_f16 v240, v144, v238, v1 op_sel_hi:[0,1,0]
	v_mfma_f32_16x16x32_f16 v[230:233], v[46:49], v[226:229], v[230:233]
	v_add_f32_e32 v144, 1.0, v145
	v_add_f32_e32 v1, 1.0, v146
	v_rcp_f32_e32 v150, v144
	v_mfma_f32_16x16x32_f16 v[158:161], v[50:53], v[186:189], v[158:161]
	v_rcp_f32_e32 v1, v1
	v_add_u32_e32 v173, 0x2000, v225
	v_fma_f32 v150, v150, -2.0, 1.0
	v_mfma_f32_16x16x32_f16 v[174:177], v[74:77], v[186:189], v[174:177]
	v_fma_f32 v243, -v1, v150, v150
	v_mfma_f32_16x16x32_f16 v[226:229], v[18:21], v[186:189], v[230:233]
	ds_read_b128 v[186:189], v142 offset:0x2000
	s_waitcnt lgkmcnt(5)
	s_nop 0
	v_mfma_f32_16x16x32_f16 v[158:161], v[10:13], v[164:167], v[158:161]
	v_mfma_f32_16x16x32_f16 v[144:147], v[90:93], v[164:167], v[174:177]
	v_mfma_f32_16x16x32_f16 v[226:229], v[58:61], v[164:167], v[226:229]
	s_mov_b32 m0, s35
	ds_read_b128 v[230:233], v201 offset:0x3000
	s_waitcnt lgkmcnt(4)
	v_exp_f32_e32 v150, v152
	v_mfma_f32_16x16x32_f16 v[164:167], v[14:17], v[178:181], v[158:161]
	ds_read_b128 v[160:163], v202 offset:0x3000
	s_waitcnt lgkmcnt(4)
	global_load_lds_dwordx4 v242, s[12:13]
	v_exp_f32_e32 v154, v153
	v_add_f32_e32 v150, 1.0, v150
	v_rcp_f32_e32 v150, v150
	v_mfma_f32_16x16x32_f16 v[174:177], v[22:25], v[178:181], v[226:229]
	v_add_f32_e32 v154, 1.0, v154
	v_rcp_f32_e32 v154, v154
	v_exp_f32_e32 v151, v156
	v_mfma_f32_16x16x32_f16 v[178:181], v[86:89], v[178:181], v[130:133]
	v_fma_f32 v148, v150, v170, v148
	v_exp_f32_e32 v148, v148
	v_fmac_f32_e32 v149, v154, v171
	v_mfma_f32_16x16x32_f16 v[226:229], v[26:29], v[182:185], v[164:167]
	v_exp_f32_e32 v149, v149
	v_add_f32_e32 v150, 1.0, v151
	v_rcp_f32_e32 v241, v150
	v_mfma_f32_16x16x32_f16 v[174:177], v[34:37], v[182:185], v[174:177]
	v_add_f32_e32 v148, 1.0, v148
	ds_read_b128 v[164:167], v203 offset:0x3000
	s_waitcnt lgkmcnt(4)
	v_mfma_f32_16x16x32_f16 v[178:181], v[78:81], v[182:185], v[178:181]
	v_exp_f32_e32 v155, v157
	v_rcp_f32_e32 v148, v148
	v_add_f32_e32 v149, 1.0, v149
	v_mfma_f32_16x16x32_f16 v[150:153], v[30:33], v[234:237], v[226:229]
	v_rcp_f32_e32 v149, v149
	ds_read_b128 v[168:171], v204 offset:0x3000
	s_waitcnt lgkmcnt(4)
	v_mfma_f32_16x16x32_f16 v[174:177], v[38:41], v[234:237], v[174:177]
	v_fma_f32 v148, v148, -2.0, 1.0
	v_fma_f32 v148, -v241, v148, v148
	v_fma_mixlo_f16 v241, v241, v239, v148 op_sel_hi:[0,1,0]
	v_mfma_f32_16x16x32_f16 v[178:181], v[82:85], v[234:237], v[178:181]
	v_fma_mixhi_f16 v240, v1, v238, v243 op_sel:[0,1,0] op_sel_hi:[0,1,0]
	v_mfma_f32_16x16x32_f16 v[156:159], v[54:57], v[186:189], v[150:153]
	s_nop 2
	v_add_f32_e32 v150, 1.0, v155
	v_mfma_f32_16x16x32_f16 v[152:155], v[62:65], v[186:189], v[174:177]
	s_nop 2
	v_rcp_f32_e32 v174, v150
	v_fma_f32 v175, v149, -2.0, 1.0
	v_mfma_f32_16x16x32_f16 v[148:151], v[94:97], v[186:189], v[178:181]
	v_fma_f32 v175, -v174, v175, v175
	v_fma_mixhi_f16 v241, v174, v239, v175 op_sel:[0,1,0] op_sel_hi:[0,1,0]
	global_store_dwordx2 v173, v[240:241], s[0:1] nt
	ds_read_b64 v[188:189], v0 offset:0x2000
	ds_read_b64 v[0:1], v0 offset:0x3000
	ds_read_b128 v[172:175], v172 offset:0x3000
	s_waitcnt lgkmcnt(6)
	s_andn2_b64 vcc, exec, s[10:11]
	v_mfma_f32_16x16x32_f16 v[180:183], v[2:5], v[230:233], v[118:121]
	s_waitcnt vmcnt(14)
	v_mfma_f32_16x16x32_f16 v[176:179], v[42:45], v[230:233], v[122:125]
	v_mfma_f32_16x16x32_f16 v[184:187], v[66:69], v[230:233], v[126:129]
	s_cbranch_vccnz .LBB5_11
	v_cvt_f16_f32_e32 v226, v134
	v_cvt_f16_f32_e32 v227, v135
	v_cvt_f16_f32_e32 v228, v136
	v_cvt_f16_f32_e32 v229, v137
	v_cvt_f16_f32_e32 v230, v138
	v_cvt_f16_f32_e32 v231, v139
	v_cvt_f16_f32_e32 v232, v140
	v_cvt_f16_f32_e32 v233, v141
	v_cmp_gt_i32_e32 vcc, s8, v224
	s_nop 1
	v_cndmask_b32_e32 v224, 0, v226, vcc
	v_cndmask_b32_e32 v226, 0, v227, vcc
	v_cndmask_b32_e32 v227, 0, v228, vcc
	v_cndmask_b32_e32 v234, 0, v229, vcc
	v_cndmask_b32_e32 v228, 0, v230, vcc
	v_cndmask_b32_e32 v230, 0, v231, vcc
	v_cndmask_b32_e32 v229, 0, v232, vcc
	v_cndmask_b32_e32 v231, 0, v233, vcc
	v_pack_b32_f16 v229, v229, v231
	v_pack_b32_f16 v228, v228, v230
	v_pack_b32_f16 v227, v227, v234
	v_pack_b32_f16 v226, v224, v226
	ds_write_b128 v220, v[226:229]
	s_branch .LBB5_11
.LBB5_16:
	v_exp_f32_e32 v2, v146
	v_exp_f32_e32 v4, v147
	v_exp_f32_e32 v3, v150
	v_exp_f32_e32 v6, v151
	v_add_f32_e32 v2, 1.0, v2
	v_rcp_f32_e32 v2, v2
	v_add_f32_e32 v4, 1.0, v4
	v_rcp_f32_e32 v4, v4
	v_add_f32_e32 v3, 1.0, v3
	v_fma_f32 v2, v154, v2, v142
	v_exp_f32_e32 v5, v2
	v_fma_f32 v2, v155, v4, v143
	v_exp_f32_e32 v7, v2
	v_rcp_f32_e32 v2, v3
	v_add_f32_e32 v3, 1.0, v5
	v_rcp_f32_e32 v4, v3
	v_add_f32_e32 v3, 1.0, v7
	v_rcp_f32_e32 v5, v3
	v_add_f32_e32 v3, 1.0, v6
	v_rcp_f32_e32 v3, v3
	v_cvt_f32_f16_sdwa v7, v0 dst_sel:DWORD dst_unused:UNUSED_PAD src0_sel:WORD_1
	v_cvt_f32_f16_e32 v6, v0
	v_pk_fma_f32 v[4:5], v[4:5], 2.0, 1.0 op_sel_hi:[1,0,0] neg_lo:[1,0,0] neg_hi:[1,0,0]
	v_exp_f32_e32 v8, v148
	v_pk_fma_f32 v[4:5], v[2:3], v[4:5], v[4:5] neg_lo:[1,0,0] neg_hi:[1,0,0]
	v_cvt_f32_f16_sdwa v9, v1 dst_sel:DWORD dst_unused:UNUSED_PAD src0_sel:WORD_1
	v_pk_fma_f32 v[2:3], v[2:3], v[6:7], v[4:5]
	v_exp_f32_e32 v4, v149
	v_add_f32_e32 v0, 1.0, v8
	v_rcp_f32_e32 v0, v0
	v_exp_f32_e32 v8, v152
	v_add_f32_e32 v4, 1.0, v4
	v_rcp_f32_e32 v6, v4
	v_fma_f32 v0, v156, v0, v144
	v_add_f32_e32 v5, 1.0, v8
	v_exp_f32_e32 v0, v0
	v_rcp_f32_e32 v4, v5
	v_exp_f32_e32 v5, v153
	v_fmac_f32_e32 v145, v157, v6
	v_exp_f32_e32 v7, v145
	v_add_f32_e32 v0, 1.0, v0
	v_rcp_f32_e32 v6, v0
	v_add_f32_e32 v0, 1.0, v5
	v_rcp_f32_e32 v5, v0
	v_add_f32_e32 v0, 1.0, v7
	v_rcp_f32_e32 v7, v0
	v_cvt_f32_f16_e32 v8, v1
	v_cvt_pk_f16_f32 v0, v2, v3
	s_lshl_b32 s2, s28, 14
	v_pk_fma_f32 v[2:3], v[6:7], 2.0, 1.0 op_sel_hi:[1,0,0] neg_lo:[1,0,0] neg_hi:[1,0,0]
	v_or_b32_e32 v10, v195, v206
	v_pk_fma_f32 v[2:3], v[4:5], v[2:3], v[2:3] neg_lo:[1,0,0] neg_hi:[1,0,0]
	s_add_i32 s2, s2, s15
	v_pk_fma_f32 v[2:3], v[4:5], v[8:9], v[2:3]
	s_nop 0
	v_cvt_pk_f16_f32 v1, v2, v3
	v_add_u32_e32 v2, s2, v10
	v_add_u32_e32 v2, 0x3000, v2
	global_store_dwordx2 v2, v[0:1], s[0:1] nt
	s_cmp_lg_u32 s43, 0
	s_cbranch_scc1 .Lmp0_row0_done
	v_mbcnt_lo_u32_b32 v4, -1, 0
	v_mbcnt_hi_u32_b32 v4, -1, v4
	v_cmp_gt_u32_e32 vcc, 4, v4
	s_and_saveexec_b64 s[44:45], vcc
	v_lshlrev_b32_e32 v4, 3, v4
	v_lshl_add_u32 v4, s42, 5, v4
	v_mov_b32_e32 v5, 0
	v_mov_b32_e32 v6, 0
	v_mov_b32_e32 v7, 0
	global_store_dwordx2 v4, v[6:7], s[0:1] nt
	s_or_b64 exec, exec, s[44:45]

	.amdhsa_kernel _Z10mp2_kernelILb0ELi0EEvPKDF16_PDF16_PKiPKfPKDv8_DF16_S6_S6_ii
		.amdhsa_group_segment_fixed_size 0
		.amdhsa_private_segment_fixed_size 0
		.amdhsa_kernarg_size 320
		.amdhsa_user_sgpr_count 2
		.amdhsa_user_sgpr_dispatch_ptr 0
		.amdhsa_user_sgpr_queue_ptr 0
		.amdhsa_user_sgpr_kernarg_segment_ptr 1
		.amdhsa_user_sgpr_dispatch_id 0
		.amdhsa_user_sgpr_kernarg_preload_length 0
		.amdhsa_user_sgpr_kernarg_preload_offset 0
		.amdhsa_user_sgpr_private_segment_size 0
		.amdhsa_uses_dynamic_stack 0
		.amdhsa_enable_private_segment 0
		.amdhsa_system_sgpr_workgroup_id_x 1
		.amdhsa_system_sgpr_workgroup_id_y 0
		.amdhsa_system_sgpr_workgroup_id_z 0
		.amdhsa_system_sgpr_workgroup_info 0
		.amdhsa_system_vgpr_workitem_id 0
		.amdhsa_next_free_vgpr 244
		.amdhsa_next_free_sgpr 46
		.amdhsa_accum_offset 244
		.amdhsa_reserve_vcc 1
		.amdhsa_float_round_mode_32 0
		.amdhsa_float_round_mode_16_64 0
		.amdhsa_float_denorm_mode_32 3
		.amdhsa_float_denorm_mode_16_64 3
		.amdhsa_dx10_clamp 1
		.amdhsa_ieee_mode 1
		.amdhsa_fp16_overflow 0
		.amdhsa_tg_split 0
		.amdhsa_exception_fp_ieee_invalid_op 0
		.amdhsa_exception_fp_denorm_src 0
		.amdhsa_exception_fp_ieee_div_zero 0
		.amdhsa_exception_fp_ieee_overflow 0
		.amdhsa_exception_fp_ieee_underflow 0
		.amdhsa_exception_fp_ieee_inexact 0
		.amdhsa_exception_int_div_zero 0
	.end_amdhsa_kernel

amdhsa.kernels:
  - .agpr_count:     0
    .args:
      - .actual_access:  write_only
        .address_space:  global
        .offset:         0
        .size:           8
        .value_kind:     global_buffer
      - .actual_access:  read_only
        .address_space:  global
        .offset:         8
        .size:           8
        .value_kind:     global_buffer
      - .actual_access:  read_only
        .address_space:  global
        .offset:         16
        .size:           8
        .value_kind:     global_buffer
      - .actual_access:  read_only
        .address_space:  global
        .offset:         24
        .size:           8
        .value_kind:     global_buffer
      - .actual_access:  read_only
        .address_space:  global
        .offset:         32
        .size:           8
        .value_kind:     global_buffer
      - .actual_access:  read_only
        .address_space:  global
        .offset:         40
        .size:           8
        .value_kind:     global_buffer
      - .actual_access:  read_only
        .address_space:  global
        .offset:         48
        .size:           8
        .value_kind:     global_buffer
      - .actual_access:  read_only
        .address_space:  global
        .offset:         56
        .size:           8
        .value_kind:     global_buffer
      - .actual_access:  read_only
        .address_space:  global
        .offset:         64
        .size:           8
        .value_kind:     global_buffer
      - .actual_access:  read_only
        .address_space:  global
        .offset:         72
        .size:           8
        .value_kind:     global_buffer
    .group_segment_fixed_size: 0
    .kernarg_segment_align: 8
    .kernarg_segment_size: 80
    .language:       OpenCL C
    .language_version:
      - 2
      - 0
    .max_flat_workgroup_size: 64
    .name:           _Z11prep_kernelPDv8_DF16_PKfS2_S2_S2_S2_S2_S2_S2_S2_
    .private_segment_fixed_size: 0
    .sgpr_count:     20
    .sgpr_spill_count: 0
    .symbol:         _Z11prep_kernelPDv8_DF16_PKfS2_S2_S2_S2_S2_S2_S2_S2_.kd
    .uniform_work_group_size: 1
    .uses_dynamic_stack: false
    .vgpr_count:     18
    .vgpr_spill_count: 0
    .wavefront_size: 64
  - .agpr_count:     0
    .args:
      - .actual_access:  read_only
        .address_space:  global
        .offset:         0
        .size:           8
        .value_kind:     global_buffer
      - .actual_access:  read_only
        .address_space:  global
        .offset:         8
        .size:           8
        .value_kind:     global_buffer
      - .actual_access:  write_only
        .address_space:  global
        .offset:         16
        .size:           8
        .value_kind:     global_buffer
    .group_segment_fixed_size: 0
    .kernarg_segment_align: 8
    .kernarg_segment_size: 24
    .language:       OpenCL C
    .language_version:
      - 2
      - 0
    .max_flat_workgroup_size: 256
    .name:           _Z11init_kernelPKfS0_PDF16_
    .private_segment_fixed_size: 0
    .sgpr_count:     16
    .sgpr_spill_count: 0
    .symbol:         _Z11init_kernelPKfS0_PDF16_.kd
    .uniform_work_group_size: 1
    .uses_dynamic_stack: false
    .vgpr_count:     118
    .vgpr_spill_count: 0
    .wavefront_size: 64
  - .agpr_count:     0
    .args:
      - .actual_access:  read_only
        .address_space:  global
        .offset:         0
        .size:           8
        .value_kind:     global_buffer
      - .actual_access:  write_only
        .address_space:  global
        .offset:         8
        .size:           8
        .value_kind:     global_buffer
      - .actual_access:  read_only
        .address_space:  global
        .offset:         16
        .size:           8
        .value_kind:     global_buffer
      - .actual_access:  read_only
        .address_space:  global
        .offset:         24
        .size:           8
        .value_kind:     global_buffer
      - .actual_access:  read_only
        .address_space:  global
        .offset:         32
        .size:           8
        .value_kind:     global_buffer
      - .actual_access:  read_only
        .address_space:  global
        .offset:         40
        .size:           8
        .value_kind:     global_buffer
      - .actual_access:  read_only
        .address_space:  global
        .offset:         48
        .size:           8
        .value_kind:     global_buffer
      - .offset:         56
        .size:           4
        .value_kind:     by_value
      - .offset:         64
        .size:           4
        .value_kind:     hidden_block_count_x
      - .offset:         68
        .size:           4
        .value_kind:     hidden_block_count_y
      - .offset:         72
        .size:           4
        .value_kind:     hidden_block_count_z
      - .offset:         76
        .size:           2
        .value_kind:     hidden_group_size_x
      - .offset:         78
        .size:           2
        .value_kind:     hidden_group_size_y
      - .offset:         80
        .size:           2
        .value_kind:     hidden_group_size_z
      - .offset:         82
        .size:           2
        .value_kind:     hidden_remainder_x
      - .offset:         84
        .size:           2
        .value_kind:     hidden_remainder_y
      - .offset:         86
        .size:           2
        .value_kind:     hidden_remainder_z
      - .offset:         104
        .size:           8
        .value_kind:     hidden_global_offset_x
      - .offset:         112
        .size:           8
        .value_kind:     hidden_global_offset_y
      - .offset:         120
        .size:           8
        .value_kind:     hidden_global_offset_z
      - .offset:         128
        .size:           2
        .value_kind:     hidden_grid_dims
      - .offset:         184
        .size:           4
        .value_kind:     hidden_dynamic_lds_size
    .group_segment_fixed_size: 0
    .kernarg_segment_align: 8
    .kernarg_segment_size: 320
    .language:       OpenCL C
    .language_version:
      - 2
      - 0
    .max_flat_workgroup_size: 512
    .name:           _Z12xproj_kernelPKDF16_PDF16_PKDv8_DF16_PKfS6_S6_S6_i
    .private_segment_fixed_size: 0
    .sgpr_count:     30
    .sgpr_spill_count: 0
    .symbol:         _Z12xproj_kernelPKDF16_PDF16_PKDv8_DF16_PKfS6_S6_S6_i.kd
    .uniform_work_group_size: 1
    .uses_dynamic_stack: false
    .vgpr_count:     16
    .vgpr_spill_count: 0
    .wavefront_size: 64
  - .agpr_count:     0
    .args:
      - .actual_access:  read_only
        .address_space:  global
        .offset:         0
        .size:           8
        .value_kind:     global_buffer
      - .actual_access:  read_only
        .address_space:  global
        .offset:         8
        .size:           8
        .value_kind:     global_buffer
      - .actual_access:  write_only
        .address_space:  global
        .offset:         16
        .size:           8
        .value_kind:     global_buffer
    .group_segment_fixed_size: 5120
    .kernarg_segment_align: 8
    .kernarg_segment_size: 24
    .language:       OpenCL C
    .language_version:
      - 2
      - 0
    .max_flat_workgroup_size: 1024
    .name:           _Z11lstm_kernelPKDF16_PKDv8_DF16_Pf
    .private_segment_fixed_size: 0
    .sgpr_count:     18
    .sgpr_spill_count: 0
    .symbol:         _Z11lstm_kernelPKDF16_PKDv8_DF16_Pf.kd
    .uniform_work_group_size: 1
    .uses_dynamic_stack: false
    .vgpr_count:     52
    .vgpr_spill_count: 0
    .wavefront_size: 64
  - .agpr_count:     0
    .args:
      - .actual_access:  read_only
        .address_space:  global
        .offset:         0
        .size:           8
        .value_kind:     global_buffer
      - .actual_access:  read_only
        .address_space:  global
        .offset:         8
        .size:           8
        .value_kind:     global_buffer
      - .actual_access:  write_only
        .address_space:  global
        .offset:         16
        .size:           8
        .value_kind:     global_buffer
    .group_segment_fixed_size: 36096
    .kernarg_segment_align: 8
    .kernarg_segment_size: 24
    .language:       OpenCL C
    .language_version:
      - 2
      - 0
    .max_flat_workgroup_size: 256
    .name:           _Z12lstm2_kernelPKDF16_PKDv8_DF16_Pf
    .private_segment_fixed_size: 0
    .sgpr_count:     38
    .sgpr_spill_count: 0
    .symbol:         _Z12lstm2_kernelPKDF16_PKDv8_DF16_Pf.kd
    .uniform_work_group_size: 1
    .uses_dynamic_stack: false
    .vgpr_count:     252
    .vgpr_spill_count: 0
    .wavefront_size: 64
  - .agpr_count:     0
    .args:
      - .address_space:  global
        .offset:         0
        .size:           8
        .value_kind:     global_buffer
      - .actual_access:  write_only
        .address_space:  global
        .offset:         8
        .size:           8
        .value_kind:     global_buffer
      - .address_space:  global
        .offset:         16
        .size:           8
        .value_kind:     global_buffer
      - .address_space:  global
        .offset:         24
        .size:           8
        .value_kind:     global_buffer
      - .actual_access:  read_only
        .address_space:  global
        .offset:         32
        .size:           8
        .value_kind:     global_buffer
      - .actual_access:  read_only
        .address_space:  global
        .offset:         40
        .size:           8
        .value_kind:     global_buffer
      - .actual_access:  read_only
        .address_space:  global
        .offset:         48
        .size:           8
        .value_kind:     global_buffer
      - .offset:         56
        .size:           4
        .value_kind:     by_value
      - .offset:         60
        .size:           4
        .value_kind:     by_value
      - .offset:         64
        .size:           4
        .value_kind:     hidden_block_count_x
      - .offset:         68
        .size:           4
        .value_kind:     hidden_block_count_y
      - .offset:         72
        .size:           4
        .value_kind:     hidden_block_count_z
      - .offset:         76
        .size:           2
        .value_kind:     hidden_group_size_x
      - .offset:         78
        .size:           2
        .value_kind:     hidden_group_size_y
      - .offset:         80
        .size:           2
        .value_kind:     hidden_group_size_z
      - .offset:         82
        .size:           2
        .value_kind:     hidden_remainder_x
      - .offset:         84
        .size:           2
        .value_kind:     hidden_remainder_y
      - .offset:         86
        .size:           2
        .value_kind:     hidden_remainder_z
      - .offset:         104
        .size:           8
        .value_kind:     hidden_global_offset_x
      - .offset:         112
        .size:           8
        .value_kind:     hidden_global_offset_y
      - .offset:         120
        .size:           8
        .value_kind:     hidden_global_offset_z
      - .offset:         128
        .size:           2
        .value_kind:     hidden_grid_dims
      - .offset:         184
        .size:           4
        .value_kind:     hidden_dynamic_lds_size
    .group_segment_fixed_size: 0
    .kernarg_segment_align: 8
    .kernarg_segment_size: 320
    .language:       OpenCL C
    .language_version:
      - 2
      - 0
    .max_flat_workgroup_size: 512
    .name:           _Z10mp2_kernelILb0ELi0EEvPKDF16_PDF16_PKiPKfPKDv8_DF16_S6_S6_ii
    .private_segment_fixed_size: 0
    .sgpr_count:     52
    .sgpr_spill_count: 0
    .symbol:         _Z10mp2_kernelILb0ELi0EEvPKDF16_PDF16_PKiPKfPKDv8_DF16_S6_S6_ii.kd
    .uniform_work_group_size: 1
    .uses_dynamic_stack: false
    .vgpr_count:     244
    .vgpr_spill_count: 0
    .wavefront_size: 64
  - .agpr_count:     0
    .args:
      - .actual_access:  read_only
        .address_space:  global
        .offset:         0
        .size:           8
        .value_kind:     global_buffer
      - .actual_access:  write_only
        .address_space:  global
        .offset:         8
        .size:           8
        .value_kind:     global_buffer
      - .address_space:  global
        .offset:         16
        .size:           8
        .value_kind:     global_buffer
      - .address_space:  global
        .offset:         24
        .size:           8
        .value_kind:     global_buffer
      - .actual_access:  read_only
        .address_space:  global
        .offset:         32
        .size:           8
        .value_kind:     global_buffer
      - .actual_access:  read_only
        .address_space:  global
        .offset:         40
        .size:           8
        .value_kind:     global_buffer
      - .actual_access:  read_only
        .address_space:  global
        .offset:         48
        .size:           8
        .value_kind:     global_buffer
      - .offset:         56
        .size:           4
        .value_kind:     by_value
      - .offset:         60
        .size:           4
        .value_kind:     by_value
      - .offset:         64
        .size:           4
        .value_kind:     hidden_block_count_x
      - .offset:         68
        .size:           4
        .value_kind:     hidden_block_count_y
      - .offset:         72
        .size:           4
        .value_kind:     hidden_block_count_z
      - .offset:         76
        .size:           2
        .value_kind:     hidden_group_size_x
      - .offset:         78
        .size:           2
        .value_kind:     hidden_group_size_y
      - .offset:         80
        .size:           2
        .value_kind:     hidden_group_size_z
      - .offset:         82
        .size:           2
        .value_kind:     hidden_remainder_x
      - .offset:         84
        .size:           2
        .value_kind:     hidden_remainder_y
      - .offset:         86
        .size:           2
        .value_kind:     hidden_remainder_z
      - .offset:         104
        .size:           8
        .value_kind:     hidden_global_offset_x
      - .offset:         112
        .size:           8
        .value_kind:     hidden_global_offset_y
      - .offset:         120
        .size:           8
        .value_kind:     hidden_global_offset_z
      - .offset:         128
        .size:           2
        .value_kind:     hidden_grid_dims
      - .offset:         184
        .size:           4
        .value_kind:     hidden_dynamic_lds_size
    .group_segment_fixed_size: 0
    .kernarg_segment_align: 8
    .kernarg_segment_size: 320
    .language:       OpenCL C
    .language_version:
      - 2
      - 0
    .max_flat_workgroup_size: 512
    .name:           _Z10mp2_kernelILb0ELi1EEvPKDF16_PDF16_PKiPKfPKDv8_DF16_S6_S6_ii
    .private_segment_fixed_size: 0
    .sgpr_count:     30
    .sgpr_spill_count: 0
    .symbol:         _Z10mp2_kernelILb0ELi1EEvPKDF16_PDF16_PKiPKfPKDv8_DF16_S6_S6_ii.kd
    .uniform_work_group_size: 1
    .uses_dynamic_stack: false
    .vgpr_count:     234
    .vgpr_spill_count: 0
    .wavefront_size: 64
  - .agpr_count:     0
    .args:
      - .address_space:  global
        .offset:         0
        .size:           8
        .value_kind:     global_buffer
      - .actual_access:  write_only
        .address_space:  global
        .offset:         8
        .size:           8
        .value_kind:     global_buffer
      - .actual_access:  read_only
        .address_space:  global
        .offset:         16
        .size:           8
        .value_kind:     global_buffer
      - .actual_access:  read_only
        .address_space:  global
        .offset:         24
        .size:           8
        .value_kind:     global_buffer
      - .actual_access:  read_only
        .address_space:  global
        .offset:         32
        .size:           8
        .value_kind:     global_buffer
      - .actual_access:  read_only
        .address_space:  global
        .offset:         40
        .size:           8
        .value_kind:     global_buffer
      - .actual_access:  read_only
        .address_space:  global
        .offset:         48
        .size:           8
        .value_kind:     global_buffer
      - .offset:         56
        .size:           4
        .value_kind:     by_value
      - .offset:         60
        .size:           4
        .value_kind:     by_value
      - .offset:         64
        .size:           4
        .value_kind:     hidden_block_count_x
      - .offset:         68
        .size:           4
        .value_kind:     hidden_block_count_y
      - .offset:         72
        .size:           4
        .value_kind:     hidden_block_count_z
      - .offset:         76
        .size:           2
        .value_kind:     hidden_group_size_x
      - .offset:         78
        .size:           2
        .value_kind:     hidden_group_size_y
      - .offset:         80
        .size:           2
        .value_kind:     hidden_group_size_z
      - .offset:         82
        .size:           2
        .value_kind:     hidden_remainder_x
      - .offset:         84
        .size:           2
        .value_kind:     hidden_remainder_y
      - .offset:         86
        .size:           2
        .value_kind:     hidden_remainder_z
      - .offset:         104
        .size:           8
        .value_kind:     hidden_global_offset_x
      - .offset:         112
        .size:           8
        .value_kind:     hidden_global_offset_y
      - .offset:         120
        .size:           8
        .value_kind:     hidden_global_offset_z
      - .offset:         128
        .size:           2
        .value_kind:     hidden_grid_dims
      - .offset:         184
        .size:           4
        .value_kind:     hidden_dynamic_lds_size
    .group_segment_fixed_size: 0
    .kernarg_segment_align: 8
    .kernarg_segment_size: 320
    .language:       OpenCL C
    .language_version:
      - 2
      - 0
    .max_flat_workgroup_size: 512
    .name:           _Z9mp_kernelILi1EEvPKDF16_PDF16_PKiPKfPKDv8_DF16_S6_S6_ii
    .private_segment_fixed_size: 0
    .sgpr_count:     46
    .sgpr_spill_count: 0
    .symbol:         _Z9mp_kernelILi1EEvPKDF16_PDF16_PKiPKfPKDv8_DF16_S6_S6_ii.kd
    .uniform_work_group_size: 1
    .uses_dynamic_stack: false
    .vgpr_count:     70
    .vgpr_spill_count: 0
    .wavefront_size: 64
  - .agpr_count:     0
    .args:
      - .address_space:  global
        .offset:         0
        .size:           8
        .value_kind:     global_buffer
      - .actual_access:  write_only
        .address_space:  global
        .offset:         8
        .size:           8
        .value_kind:     global_buffer
      - .address_space:  global
        .offset:         16
        .size:           8
        .value_kind:     global_buffer
      - .address_space:  global
        .offset:         24
        .size:           8
        .value_kind:     global_buffer
      - .actual_access:  read_only
        .address_space:  global
        .offset:         32
        .size:           8
        .value_kind:     global_buffer
      - .actual_access:  read_only
        .address_space:  global
        .offset:         40
        .size:           8
        .value_kind:     global_buffer
      - .actual_access:  read_only
        .address_space:  global
        .offset:         48
        .size:           8
        .value_kind:     global_buffer
      - .offset:         56
        .size:           4
        .value_kind:     by_value
      - .offset:         60
        .size:           4
        .value_kind:     by_value
      - .offset:         64
        .size:           4
        .value_kind:     hidden_block_count_x
      - .offset:         68
        .size:           4
        .value_kind:     hidden_block_count_y
      - .offset:         72
        .size:           4
        .value_kind:     hidden_block_count_z
      - .offset:         76
        .size:           2
        .value_kind:     hidden_group_size_x
      - .offset:         78
        .size:           2
        .value_kind:     hidden_group_size_y
      - .offset:         80
        .size:           2
        .value_kind:     hidden_group_size_z
      - .offset:         82
        .size:           2
        .value_kind:     hidden_remainder_x
      - .offset:         84
        .size:           2
        .value_kind:     hidden_remainder_y
      - .offset:         86
        .size:           2
        .value_kind:     hidden_remainder_z
      - .offset:         104
        .size:           8
        .value_kind:     hidden_global_offset_x
      - .offset:         112
        .size:           8
        .value_kind:     hidden_global_offset_y
      - .offset:         120
        .size:           8
        .value_kind:     hidden_global_offset_z
      - .offset:         128
        .size:           2
        .value_kind:     hidden_grid_dims
      - .offset:         184
        .size:           4
        .value_kind:     hidden_dynamic_lds_size
    .group_segment_fixed_size: 0
    .kernarg_segment_align: 8
    .kernarg_segment_size: 320
    .language:       OpenCL C
    .language_version:
      - 2
      - 0
    .max_flat_workgroup_size: 512
    .name:           _Z10mp2_kernelILb0ELi2EEvPKDF16_PDF16_PKiPKfPKDv8_DF16_S6_S6_ii
    .private_segment_fixed_size: 0
    .sgpr_count:     32
    .sgpr_spill_count: 0
    .symbol:         _Z10mp2_kernelILb0ELi2EEvPKDF16_PDF16_PKiPKfPKDv8_DF16_S6_S6_ii.kd
    .uniform_work_group_size: 1
    .uses_dynamic_stack: false
    .vgpr_count:     99
    .vgpr_spill_count: 0
    .wavefront_size: 64
